# stack8
# speedup vs baseline: 1.0025x; 1.0003x over previous
_Z7k_gemm2PK15HIP_vector_typeIjLj4EEPKS_IjLj2EEPKfS2_S2_S7_PtS8_:
	s_load_dwordx8 s[12:19], s[0:1], 0x0
	s_load_dwordx8 s[4:11], s[0:1], 0x20
	v_lshlrev_b32_e32 v2, 4, v0
	s_waitcnt lgkmcnt(0)
	s_lshl_b32 s1, s2, 10
	s_bfe_i32 s0, s2, 0x140002
	s_mov_b64 s[20:21], s[18:19]
	global_load_dwordx4 v[8:11], v2, s[20:21]
	s_add_u32 s20, s20, 0x4000
	s_addc_u32 s21, s21, 0
	global_load_dwordx4 v[12:15], v2, s[20:21]
	s_add_u32 s20, s20, 0x4000
	s_addc_u32 s21, s21, 0
	global_load_dwordx4 v[16:19], v2, s[20:21]
	s_add_u32 s20, s20, 0x4000
	s_addc_u32 s21, s21, 0
	global_load_dwordx4 v[20:23], v2, s[20:21]
	s_add_u32 s20, s20, 0x4000
	s_addc_u32 s21, s21, 0
	global_load_dwordx4 v[24:27], v2, s[20:21]
	s_add_u32 s20, s20, 0x4000
	s_addc_u32 s21, s21, 0
	global_load_dwordx4 v[28:31], v2, s[20:21]
	s_add_u32 s20, s20, 0x4000
	s_addc_u32 s21, s21, 0
	s_add_u32 s22, s4, 0x13000
	s_addc_u32 s23, s5, 0
	global_load_dwordx4 v[32:35], v2, s[22:23]
	v_cmp_gt_u32_e32 vcc, 0x100, v0
	s_and_saveexec_b64 s[24:25], vcc
	global_load_dwordx4 v[36:39], v2, s[20:21]
	s_mov_b64 exec, s[24:25]
	v_cmp_gt_u32_e32 vcc, 0x200, v0
	s_add_u32 s22, s22, 0x4000
	s_addc_u32 s23, s23, 0
	s_and_saveexec_b64 s[24:25], vcc
	global_load_dwordx4 v[40:43], v2, s[22:23]
	s_mov_b64 exec, s[24:25]
	v_cmp_gt_u32_e32 vcc, 0x64, v0
	s_mul_i32 s26, s0, 0x190
	s_add_u32 s22, s16, s26
	s_addc_u32 s23, s17, 0
	v_lshlrev_b32_e32 v3, 2, v0
	s_and_saveexec_b64 s[24:25], vcc
	global_load_dword v44, v3, s[22:23]
	s_mov_b64 exec, s[24:25]
	v_add_u32_e32 v4, 0x10000, v2
	v_add_u32_e32 v5, 0x19000, v2
	v_mov_b32_e32 v6, 0x1f000
	v_lshl_or_b32 v6, v0, 2, v6
	s_waitcnt vmcnt(0)
	ds_write_b128 v2, v[8:11]
	ds_write_b128 v2, v[12:15] offset:16384
	ds_write_b128 v2, v[16:19] offset:32768
	ds_write_b128 v2, v[20:23] offset:49152
	ds_write_b128 v4, v[24:27]
	ds_write_b128 v4, v[28:31] offset:16384
	ds_write_b128 v5, v[32:35]
	v_cmp_gt_u32_e32 vcc, 0x100, v0
	s_and_saveexec_b64 s[24:25], vcc
	ds_write_b128 v4, v[36:39] offset:32768
	s_mov_b64 exec, s[24:25]
	v_cmp_gt_u32_e32 vcc, 0x200, v0
	s_and_saveexec_b64 s[24:25], vcc
	ds_write_b128 v5, v[40:43] offset:16384
	s_mov_b64 exec, s[24:25]
	v_cmp_gt_u32_e32 vcc, 0x64, v0
	s_and_saveexec_b64 s[24:25], vcc
	ds_write_b32 v6, v44
	s_mov_b64 exec, s[24:25]
	v_mov_b32_e32 v1, 0xfc0
	v_bfe_u32 v97, v0, 5, 1
	v_bitop3_b32 v98, s1, v1, v0 bitop3:0xc8
	s_mul_i32 s1, s0, 24
	v_and_b32_e32 v96, 31, v0
	v_or_b32_e32 v0, s1, v97
	v_ashrrev_i32_e32 v1, 31, v0
	v_lshlrev_b64 v[0:1], 16, v[0:1]
	v_lshl_add_u64 v[0:1], s[12:13], 0, v[0:1]
	v_mov_b32_e32 v49, 0
	v_lshlrev_b32_e32 v48, 4, v98
	v_lshl_add_u64 v[0:1], v[0:1], 0, v[48:49]
	v_lshlrev_b32_e32 v48, 4, v96
	v_lshl_add_u64 v[100:101], v[0:1], 0, v[48:49]
	s_mov_b64 s[2:3], 0x160000
	v_lshl_add_u64 v[0:1], v[100:101], 0, s[2:3]
	s_mov_b64 s[2:3], 0x160200
	s_waitcnt lgkmcnt(0)
	s_barrier
	global_load_dwordx4 v[72:75], v[0:1], off
	v_lshl_add_u64 v[0:1], v[100:101], 0, s[2:3]
	s_mov_b64 s[2:3], 0x140000
	global_load_dwordx4 v[64:67], v[0:1], off
	v_lshl_add_u64 v[0:1], v[100:101], 0, s[2:3]
	s_mov_b64 s[2:3], 0x140200
	global_load_dwordx4 v[76:79], v[0:1], off
	v_lshl_add_u64 v[0:1], v[100:101], 0, s[2:3]
	v_lshlrev_b32_e32 v99, 2, v97
	v_lshl_or_b32 v102, v97, 10, v48
	global_load_dwordx4 v[68:71], v[0:1], off
	s_mov_b32 s2, -2
	s_mov_b32 s3, 0
	s_mov_b64 s[4:5], 0x200
	v_mov_b32_e32 v103, v102
	v_mov_b32_e32 v104, v99
	v_mov_b32_e32 v48, v49
	v_mov_b32_e32 v50, v49
	v_mov_b32_e32 v51, v49
	v_mov_b32_e32 v52, v49
	v_mov_b32_e32 v53, v49
	v_mov_b32_e32 v54, v49
	v_mov_b32_e32 v55, v49
	v_mov_b32_e32 v56, v49
	v_mov_b32_e32 v57, v49
	v_mov_b32_e32 v58, v49
	v_mov_b32_e32 v59, v49
	v_mov_b32_e32 v60, v49
	v_mov_b32_e32 v61, v49
	v_mov_b32_e32 v62, v49
	v_mov_b32_e32 v63, v49
	v_mov_b32_e32 v32, v49
	v_mov_b32_e32 v33, v49
	v_mov_b32_e32 v34, v49
	v_mov_b32_e32 v35, v49
	v_mov_b32_e32 v36, v49
	v_mov_b32_e32 v37, v49
	v_mov_b32_e32 v38, v49
	v_mov_b32_e32 v39, v49
	v_mov_b32_e32 v40, v49
	v_mov_b32_e32 v41, v49
	v_mov_b32_e32 v42, v49
	v_mov_b32_e32 v43, v49
	v_mov_b32_e32 v44, v49
	v_mov_b32_e32 v45, v49
	v_mov_b32_e32 v46, v49
	v_mov_b32_e32 v47, v49
	v_mov_b32_e32 v16, v49
	v_mov_b32_e32 v17, v49
	v_mov_b32_e32 v18, v49
	v_mov_b32_e32 v19, v49
	v_mov_b32_e32 v20, v49
	v_mov_b32_e32 v21, v49
	v_mov_b32_e32 v22, v49
	v_mov_b32_e32 v23, v49
	v_mov_b32_e32 v24, v49
	v_mov_b32_e32 v25, v49
	v_mov_b32_e32 v26, v49
	v_mov_b32_e32 v27, v49
	v_mov_b32_e32 v28, v49
	v_mov_b32_e32 v29, v49
	v_mov_b32_e32 v30, v49
	v_mov_b32_e32 v31, v49
	v_mov_b32_e32 v0, v49
	v_mov_b32_e32 v1, v49
	v_mov_b32_e32 v2, v49
	v_mov_b32_e32 v3, v49
	v_mov_b32_e32 v4, v49
	v_mov_b32_e32 v5, v49
	v_mov_b32_e32 v6, v49
	v_mov_b32_e32 v7, v49
	v_mov_b32_e32 v8, v49
	v_mov_b32_e32 v9, v49
	v_mov_b32_e32 v10, v49
	v_mov_b32_e32 v11, v49
	v_mov_b32_e32 v12, v49
	v_mov_b32_e32 v13, v49
	v_mov_b32_e32 v14, v49
	v_mov_b32_e32 v15, v49
